# v59 + weight-copy chunks: waves 4-7 start ~4.9us later (2 x s_sleep 80), half of a copy-loop iteration
# speedup vs baseline: 1.0068x; 1.0006x over previous
.LBB6_901:
	s_lshl_b32 s84, s0, 3
	s_or_b32 s1, s84, s59
	s_mul_hi_i32 s3, s63, s1
	s_mul_i32 s2, s63, s1
	s_lshr_b64 s[2:3], s[2:3], 9
	s_add_i32 s1, s1, 1
	s_and_b32 s90, s2, 0xffffffe0
	s_mul_hi_i32 s3, s63, s1
	s_mul_i32 s2, s63, s1
	s_lshr_b64 s[2:3], s[2:3], 9
	s_and_b32 s91, s2, 0xffffffe0
	s_bitcmp0_b32 s0, 0
	s_cselect_b64 s[22:23], -1, 0
	s_and_b64 vcc, exec, s[22:23]
	s_cbranch_vccnz .LBB6_1210
	v_readfirstlane_b32 s98, v0
	s_nop 0
	s_bitcmp1_b32 s98, 8
	s_cbranch_scc0 .Ldephase_a
	s_sleep 80
	s_sleep 80

.LBB6_1307:
	v_readlane_b32 s6, v254, 13
	v_readlane_b32 s7, v254, 14
	s_waitcnt vmcnt(0)
	v_mov_b32_e32 v167, v0
	s_waitcnt lgkmcnt(0)
	s_barrier
	v_readfirstlane_b32 s98, v0
	s_nop 0
	s_bitcmp1_b32 s98, 8
	s_cbranch_scc0 .Ldephase_b
	s_sleep 80
	s_sleep 80

.LBB6_2087:
	s_mov_b32 s0, s96
	s_cmpk_lt_i32 s0, 0x80
	s_cbranch_scc1 .LBB6_2098
	v_readlane_b32 s2, v254, 13
	v_readlane_b32 s3, v254, 14
	v_mov_b32_e32 v135, v0
	s_waitcnt vmcnt(0) lgkmcnt(0)
	s_barrier
	v_readfirstlane_b32 s98, v0
	s_nop 0
	s_bitcmp1_b32 s98, 8
	s_cbranch_scc0 .Ldephase_c
	s_sleep 80
	s_sleep 80
